# attention: QK^T K-fragment 3-deep LDS ring with counted lgkmcnt + softmax VALU re-spaced; unit order remapped so the 16 query blocks of a head share one XCD L2
# baseline (speedup 1.0000x reference)
; __device__ __forceinline__ unsigned f2bf(float f) { unsigned u = __builtin_bit_cast(unsigned, f); return (u + 0x7fffu + ((u >> 16) & 1u)) >> 16; }
; __device__ __forceinline__ int crow(int r, int hi) { return (r & 3) + 8 * (r >> 2) + 4 * hi; }
; __device__ __forceinline__ void attn_unit(const bf16* __restrict__ Qraw, const float* __restrict__ ssq, const float* __restrict__ qn, int t0, const bf16* __restrict__ Kh, const bf16* __restrict__ Vh, bf16* __restrict__ Ob, int seq, LAS char* lds, int tid) {
;     ...
;     if (hi == 0) li_l[r32] = l_reg; asm volatile("s_waitcnt lgkmcnt(0)" ::: "memory");
;     float rli[16];
; #pragma unroll
;     for (int r = 0; r < 16; ++r) rli[r] = __builtin_amdgcn_rcpf(li_l[crow(r, hi)]);
;     char* Ow = (char*)Ob + (size_t)(wid * QBLK) * DM * 2; const unsigned ooff = (unsigned)(4 * hi * DM + r32) * 2u;
; #pragma unroll
;     for (int r = 0; r < 16; ++r) {
; #pragma unroll
;         for (int d0 = 0; d0 < 4; ++d0) *(bf16*)(Ow + (((r & 3) + 8 * (r >> 2)) * DM + d0 * 32) * 2 + ooff) = (bf16)f2bf(o[d0][r] * rli[r]); }
.LBB0_1447:
	s_or_b64 exec, exec, s[10:11]
	s_waitcnt lgkmcnt(0)
	v_add_u32_e32 v1, s58, v188
	ds_read_b128 v[66:69], v1
	ds_read_b128 v[70:73], v1 offset:32
	s_lshl_b64 s[6:7], s[6:7], 12
	s_add_u32 s6, s53, s6
	s_addc_u32 s7, s54, s7
	s_waitcnt lgkmcnt(1)
	v_rcp_f32_e32 v74, v66
	v_rcp_f32_e32 v75, v67
	v_rcp_f32_e32 v76, v68
	v_rcp_f32_e32 v77, v69
	ds_read_b128 v[66:69], v1 offset:64
	s_lshl_b32 s10, s56, 8
	s_add_u32 s10, s6, s10
	s_addc_u32 s11, s7, 0
	s_lshl_b64 s[6:7], s[8:9], 12
	v_mul_f32_e32 v2, v2, v74
	s_waitcnt lgkmcnt(1)
	v_rcp_f32_e32 v78, v70
	v_rcp_f32_e32 v79, v71
	v_rcp_f32_e32 v80, v72
	v_rcp_f32_e32 v81, v73
	ds_read_b128 v[70:73], v1 offset:96
	s_waitcnt lgkmcnt(1)
	v_rcp_f32_e32 v1, v66
	s_add_u32 s6, s10, s6
	v_lshlrev_b32_e32 v66, 1, v186
	v_bfe_u32 v83, v2, 16, 1
	s_addc_u32 s7, s11, s7
	v_lshl_or_b32 v146, v187, 14, v66
	v_add3_u32 v2, v2, v83, s37
	global_store_short_d16_hi v146, v2, s[6:7] offset:2048
	v_mul_f32_e32 v2, v50, v74
	v_bfe_u32 v50, v2, 16, 1
	v_add3_u32 v2, v2, v50, s37
	global_store_short_d16_hi v146, v2, s[6:7] offset:2112
	v_mul_f32_e32 v2, v34, v74
	v_bfe_u32 v34, v2, 16, 1
	v_add3_u32 v2, v2, v34, s37
	global_store_short_d16_hi v146, v2, s[6:7] offset:2176
	v_mul_f32_e32 v2, v18, v74
	v_bfe_u32 v18, v2, 16, 1
	v_add3_u32 v2, v2, v18, s37
	global_store_short_d16_hi v146, v2, s[6:7] offset:2240
	v_mul_f32_e32 v2, v3, v75
	v_rcp_f32_e32 v82, v67
	v_lshl_add_u64 v[66:67], s[6:7], 0, v[146:147]
	v_bfe_u32 v3, v2, 16, 1
	v_add3_u32 v18, v2, v3, s37
	v_add_co_u32_e32 v2, vcc, s87, v66
	s_movk_i32 s6, 0x3000
	s_nop 0
	v_addc_co_u32_e32 v3, vcc, 0, v67, vcc
	global_store_short_d16_hi v[2:3], v18, off offset:2048
	v_mul_f32_e32 v18, v51, v75
	v_bfe_u32 v34, v18, 16, 1
	v_add3_u32 v18, v18, v34, s37
	global_store_short_d16_hi v[2:3], v18, off offset:2112
	v_mul_f32_e32 v18, v35, v75
	v_bfe_u32 v34, v18, 16, 1
	v_add3_u32 v18, v18, v34, s37
	global_store_short_d16_hi v[2:3], v18, off offset:2176
	v_mul_f32_e32 v18, v19, v75
	v_bfe_u32 v19, v18, 16, 1
	v_add3_u32 v18, v18, v19, s37
	global_store_short_d16_hi v[2:3], v18, off offset:2240
	v_mul_f32_e32 v2, v4, v76
	v_bfe_u32 v3, v2, 16, 1
	v_add3_u32 v4, v2, v3, s37
	v_add_co_u32_e32 v2, vcc, s80, v66
	v_rcp_f32_e32 v68, v68
	s_nop 0
	v_addc_co_u32_e32 v3, vcc, 0, v67, vcc
	global_store_short_d16_hi v[2:3], v4, off offset:2048
	v_mul_f32_e32 v4, v52, v76
	v_bfe_u32 v18, v4, 16, 1
	v_add3_u32 v4, v4, v18, s37
	global_store_short_d16_hi v[2:3], v4, off offset:2112
	v_mul_f32_e32 v4, v36, v76
	v_bfe_u32 v18, v4, 16, 1
	v_add3_u32 v4, v4, v18, s37
	global_store_short_d16_hi v[2:3], v4, off offset:2176
	v_mul_f32_e32 v4, v20, v76
	v_bfe_u32 v18, v4, 16, 1
	v_add3_u32 v4, v4, v18, s37
	global_store_short_d16_hi v[2:3], v4, off offset:2240
	v_mul_f32_e32 v2, v5, v77
	v_bfe_u32 v3, v2, 16, 1
	v_add3_u32 v4, v2, v3, s37
	v_add_co_u32_e32 v2, vcc, s6, v66
	s_mov_b32 s6, 0x9000
	s_nop 0
	v_addc_co_u32_e32 v3, vcc, 0, v67, vcc
	global_store_short_d16_hi v[2:3], v4, off offset:2048
	v_mul_f32_e32 v4, v53, v77
	v_bfe_u32 v5, v4, 16, 1
	v_add3_u32 v4, v4, v5, s37
	global_store_short_d16_hi v[2:3], v4, off offset:2112
	v_mul_f32_e32 v4, v37, v77
	v_bfe_u32 v5, v4, 16, 1
	v_add3_u32 v4, v4, v5, s37
	global_store_short_d16_hi v[2:3], v4, off offset:2176
	v_mul_f32_e32 v4, v21, v77
	v_bfe_u32 v5, v4, 16, 1
	v_add3_u32 v4, v4, v5, s37
	global_store_short_d16_hi v[2:3], v4, off offset:2240
	v_mul_f32_e32 v2, v6, v78
	v_bfe_u32 v3, v2, 16, 1
	v_add3_u32 v4, v2, v3, s37
	v_add_co_u32_e32 v2, vcc, s83, v66
	v_rcp_f32_e32 v69, v69
	s_nop 0
	v_addc_co_u32_e32 v3, vcc, 0, v67, vcc
	global_store_short_d16_hi v[2:3], v4, off offset:2048
	v_mul_f32_e32 v4, v54, v78
	v_bfe_u32 v5, v4, 16, 1
	v_add3_u32 v4, v4, v5, s37
	global_store_short_d16_hi v[2:3], v4, off offset:2112
	v_mul_f32_e32 v4, v38, v78
	v_bfe_u32 v5, v4, 16, 1
	v_add3_u32 v4, v4, v5, s37
	global_store_short_d16_hi v[2:3], v4, off offset:2176
	v_mul_f32_e32 v4, v22, v78
	v_bfe_u32 v5, v4, 16, 1
	v_add3_u32 v4, v4, v5, s37
	global_store_short_d16_hi v[2:3], v4, off offset:2240
	v_mul_f32_e32 v2, v7, v79
	v_bfe_u32 v3, v2, 16, 1
	v_add3_u32 v4, v2, v3, s37
	v_add_co_u32_e32 v2, vcc, s6, v66
	s_mov_b32 s6, 0xa000
	s_nop 0
	v_addc_co_u32_e32 v3, vcc, 0, v67, vcc
	global_store_short_d16_hi v[2:3], v4, off offset:2048
	v_mul_f32_e32 v4, v55, v79
	v_bfe_u32 v5, v4, 16, 1
	v_add3_u32 v4, v4, v5, s37
	global_store_short_d16_hi v[2:3], v4, off offset:2112
	v_mul_f32_e32 v4, v39, v79
	v_bfe_u32 v5, v4, 16, 1
	v_add3_u32 v4, v4, v5, s37
	global_store_short_d16_hi v[2:3], v4, off offset:2176
	v_mul_f32_e32 v4, v23, v79
	v_bfe_u32 v5, v4, 16, 1
	v_add3_u32 v4, v4, v5, s37
	global_store_short_d16_hi v[2:3], v4, off offset:2240
	v_mul_f32_e32 v2, v8, v80
	v_bfe_u32 v3, v2, 16, 1
	v_add3_u32 v4, v2, v3, s37
	v_add_co_u32_e32 v2, vcc, s6, v66
	s_mov_b32 s6, 0xb000
	s_nop 0
	v_addc_co_u32_e32 v3, vcc, 0, v67, vcc
	global_store_short_d16_hi v[2:3], v4, off offset:2048
	v_mul_f32_e32 v4, v56, v80
	v_bfe_u32 v5, v4, 16, 1
	v_add3_u32 v4, v4, v5, s37
	global_store_short_d16_hi v[2:3], v4, off offset:2112
	v_mul_f32_e32 v4, v40, v80
	v_bfe_u32 v5, v4, 16, 1
	v_add3_u32 v4, v4, v5, s37
	global_store_short_d16_hi v[2:3], v4, off offset:2176
	v_mul_f32_e32 v4, v24, v80
	v_bfe_u32 v5, v4, 16, 1
	v_add3_u32 v4, v4, v5, s37
	global_store_short_d16_hi v[2:3], v4, off offset:2240
	v_mul_f32_e32 v2, v9, v81
	v_bfe_u32 v3, v2, 16, 1
	v_add3_u32 v4, v2, v3, s37
	v_add_co_u32_e32 v2, vcc, s6, v66
	s_mov_b32 s6, 0x11000
	s_nop 0
	v_addc_co_u32_e32 v3, vcc, 0, v67, vcc
	global_store_short_d16_hi v[2:3], v4, off offset:2048
	v_mul_f32_e32 v4, v57, v81
	v_bfe_u32 v5, v4, 16, 1
	v_add3_u32 v4, v4, v5, s37
	global_store_short_d16_hi v[2:3], v4, off offset:2112
	v_mul_f32_e32 v4, v41, v81
	v_bfe_u32 v5, v4, 16, 1
	v_add3_u32 v4, v4, v5, s37
	global_store_short_d16_hi v[2:3], v4, off offset:2176
	v_mul_f32_e32 v4, v25, v81
	v_bfe_u32 v5, v4, 16, 1
	v_add3_u32 v4, v4, v5, s37
	global_store_short_d16_hi v[2:3], v4, off offset:2240
	v_mul_f32_e32 v2, v10, v1
	v_bfe_u32 v3, v2, 16, 1
	v_add3_u32 v4, v2, v3, s37
	v_add_co_u32_e32 v2, vcc, s81, v66
	s_waitcnt lgkmcnt(0)
; __device__ __forceinline__ unsigned f2bf(float f) { unsigned u = __builtin_bit_cast(unsigned, f); return (u + 0x7fffu + ((u >> 16) & 1u)) >> 16; }
; __device__ __forceinline__ int crow(int r, int hi) { return (r & 3) + 8 * (r >> 2) + 4 * hi; }
; __device__ __forceinline__ void attn_unit(const bf16* __restrict__ Qraw, const float* __restrict__ ssq, const float* __restrict__ qn, int t0, const bf16* __restrict__ Kh, const bf16* __restrict__ Vh, bf16* __restrict__ Ob, int seq, LAS char* lds, int tid) {
;     ...
;     float rli[16];
; #pragma unroll
;     for (int r = 0; r < 16; ++r) rli[r] = __builtin_amdgcn_rcpf(li_l[crow(r, hi)]);
;     char* Ow = (char*)Ob + (size_t)(wid * QBLK) * DM * 2; const unsigned ooff = (unsigned)(4 * hi * DM + r32) * 2u;
; #pragma unroll
;     for (int r = 0; r < 16; ++r) {
; #pragma unroll
;         for (int d0 = 0; d0 < 4; ++d0) *(bf16*)(Ow + (((r & 3) + 8 * (r >> 2)) * DM + d0 * 32) * 2 + ooff) = (bf16)f2bf(o[d0][r] * rli[r]); }
;     __syncthreads();
; __device__ __forceinline__ void phase_attn(const Args& a, const Ctx& c0, int l, bool last) {
;     ...
;     for (int u = c.bid; u < nun; u += c.G) {
;         const bool isl = u < 512; const int bh = isl ? (u >> 4) : (u - 512), qb = u & 15, b = bh >> 3, h = bh & 7;
	v_rcp_f32_e32 v70, v70
	v_addc_co_u32_e32 v3, vcc, 0, v67, vcc
	global_store_short_d16_hi v[2:3], v4, off offset:2048
	v_mul_f32_e32 v4, v58, v1
	v_bfe_u32 v5, v4, 16, 1
	v_add3_u32 v4, v4, v5, s37
	global_store_short_d16_hi v[2:3], v4, off offset:2112
	v_mul_f32_e32 v4, v42, v1
	v_bfe_u32 v5, v4, 16, 1
	v_add3_u32 v4, v4, v5, s37
	v_mul_f32_e32 v1, v26, v1
	global_store_short_d16_hi v[2:3], v4, off offset:2176
	v_bfe_u32 v4, v1, 16, 1
	v_add3_u32 v1, v1, v4, s37
	global_store_short_d16_hi v[2:3], v1, off offset:2240
	v_mul_f32_e32 v1, v11, v82
	v_bfe_u32 v2, v1, 16, 1
	v_add3_u32 v1, v1, v2, s37
	v_add_co_u32_e32 v2, vcc, s6, v66
	s_mov_b32 s6, 0x12000
	s_nop 0
	v_addc_co_u32_e32 v3, vcc, 0, v67, vcc
	global_store_short_d16_hi v[2:3], v1, off offset:2048
	v_mul_f32_e32 v1, v59, v82
	v_bfe_u32 v4, v1, 16, 1
	v_add3_u32 v1, v1, v4, s37
	global_store_short_d16_hi v[2:3], v1, off offset:2112
	v_mul_f32_e32 v1, v43, v82
	v_bfe_u32 v4, v1, 16, 1
	v_add3_u32 v1, v1, v4, s37
	global_store_short_d16_hi v[2:3], v1, off offset:2176
	v_mul_f32_e32 v1, v27, v82
	v_bfe_u32 v4, v1, 16, 1
	v_add3_u32 v1, v1, v4, s37
	global_store_short_d16_hi v[2:3], v1, off offset:2240
	v_mul_f32_e32 v1, v12, v68
	v_bfe_u32 v2, v1, 16, 1
	v_add3_u32 v1, v1, v2, s37
	v_add_co_u32_e32 v2, vcc, s6, v66
	s_mov_b32 s6, 0x13000
	s_nop 0
	v_addc_co_u32_e32 v3, vcc, 0, v67, vcc
	global_store_short_d16_hi v[2:3], v1, off offset:2048
	v_mul_f32_e32 v1, v60, v68
	v_bfe_u32 v4, v1, 16, 1
	v_add3_u32 v1, v1, v4, s37
	global_store_short_d16_hi v[2:3], v1, off offset:2112
	v_mul_f32_e32 v1, v44, v68
	v_bfe_u32 v4, v1, 16, 1
	v_add3_u32 v1, v1, v4, s37
	global_store_short_d16_hi v[2:3], v1, off offset:2176
	v_mul_f32_e32 v1, v28, v68
	v_bfe_u32 v4, v1, 16, 1
	v_add3_u32 v1, v1, v4, s37
	global_store_short_d16_hi v[2:3], v1, off offset:2240
	v_mul_f32_e32 v1, v13, v69
	v_bfe_u32 v2, v1, 16, 1
	v_add3_u32 v1, v1, v2, s37
	v_add_co_u32_e32 v2, vcc, s6, v66
	v_rcp_f32_e32 v71, v71
	s_nop 0
	v_addc_co_u32_e32 v3, vcc, 0, v67, vcc
	global_store_short_d16_hi v[2:3], v1, off offset:2048
	v_mul_f32_e32 v1, v61, v69
	v_bfe_u32 v4, v1, 16, 1
	v_add3_u32 v1, v1, v4, s37
	global_store_short_d16_hi v[2:3], v1, off offset:2112
	v_mul_f32_e32 v1, v45, v69
	v_bfe_u32 v4, v1, 16, 1
	v_add3_u32 v1, v1, v4, s37
	global_store_short_d16_hi v[2:3], v1, off offset:2176
	v_mul_f32_e32 v1, v29, v69
	v_bfe_u32 v4, v1, 16, 1
	v_add3_u32 v1, v1, v4, s37
	global_store_short_d16_hi v[2:3], v1, off offset:2240
	v_mul_f32_e32 v1, v14, v70
	v_bfe_u32 v2, v1, 16, 1
	v_add3_u32 v1, v1, v2, s37
	v_add_co_u32_e32 v2, vcc, s82, v66
	s_mov_b32 s6, 0x19000
	s_nop 0
	v_addc_co_u32_e32 v3, vcc, 0, v67, vcc
	global_store_short_d16_hi v[2:3], v1, off offset:2048
	v_mul_f32_e32 v1, v62, v70
	v_bfe_u32 v4, v1, 16, 1
	v_add3_u32 v1, v1, v4, s37
	global_store_short_d16_hi v[2:3], v1, off offset:2112
	v_mul_f32_e32 v1, v46, v70
	v_bfe_u32 v4, v1, 16, 1
	v_add3_u32 v1, v1, v4, s37
	global_store_short_d16_hi v[2:3], v1, off offset:2176
	v_mul_f32_e32 v1, v30, v70
	v_bfe_u32 v4, v1, 16, 1
	v_add3_u32 v1, v1, v4, s37
	global_store_short_d16_hi v[2:3], v1, off offset:2240
	v_mul_f32_e32 v1, v15, v71
	v_bfe_u32 v2, v1, 16, 1
	v_add3_u32 v1, v1, v2, s37
	v_add_co_u32_e32 v2, vcc, s6, v66
	v_rcp_f32_e32 v72, v72
	s_nop 0
	v_addc_co_u32_e32 v3, vcc, 0, v67, vcc
	global_store_short_d16_hi v[2:3], v1, off offset:2048
	v_mul_f32_e32 v1, v63, v71
	v_bfe_u32 v4, v1, 16, 1
	v_add3_u32 v1, v1, v4, s37
	global_store_short_d16_hi v[2:3], v1, off offset:2112
	v_mul_f32_e32 v1, v47, v71
	v_bfe_u32 v4, v1, 16, 1
	v_add3_u32 v1, v1, v4, s37
	global_store_short_d16_hi v[2:3], v1, off offset:2176
	v_mul_f32_e32 v1, v31, v71
	v_bfe_u32 v4, v1, 16, 1
	v_add3_u32 v1, v1, v4, s37
	global_store_short_d16_hi v[2:3], v1, off offset:2240
	v_mul_f32_e32 v1, v16, v72
	v_bfe_u32 v2, v1, 16, 1
	s_mov_b32 s6, 0x1a000
	v_add3_u32 v1, v1, v2, s37
	v_add_co_u32_e32 v2, vcc, s6, v66
	v_rcp_f32_e32 v73, v73
	s_nop 0
	v_addc_co_u32_e32 v3, vcc, 0, v67, vcc
	global_store_short_d16_hi v[2:3], v1, off offset:2048
	v_mul_f32_e32 v1, v64, v72
	v_bfe_u32 v4, v1, 16, 1
	v_add3_u32 v1, v1, v4, s37
	global_store_short_d16_hi v[2:3], v1, off offset:2112
	v_mul_f32_e32 v1, v48, v72
	v_bfe_u32 v4, v1, 16, 1
	v_add3_u32 v1, v1, v4, s37
	global_store_short_d16_hi v[2:3], v1, off offset:2176
	v_mul_f32_e32 v1, v32, v72
	v_bfe_u32 v4, v1, 16, 1
	v_add3_u32 v1, v1, v4, s37
	global_store_short_d16_hi v[2:3], v1, off offset:2240
	v_mul_f32_e32 v1, v17, v73
	v_bfe_u32 v2, v1, 16, 1
	s_mov_b32 s6, 0x1b000
	v_add3_u32 v1, v1, v2, s37
	v_add_co_u32_e32 v2, vcc, s6, v66
	v_readlane_b32 s55, v255, 46
	s_add_i32 s55, s55, s91
	s_nop 0
	v_addc_co_u32_e32 v3, vcc, 0, v67, vcc
	global_store_short_d16_hi v[2:3], v1, off offset:2048
	v_mul_f32_e32 v1, v65, v73
	v_bfe_u32 v4, v1, 16, 1
	v_add3_u32 v1, v1, v4, s37
	global_store_short_d16_hi v[2:3], v1, off offset:2112
	v_mul_f32_e32 v1, v49, v73
	v_bfe_u32 v4, v1, 16, 1
	v_add3_u32 v1, v1, v4, s37
	global_store_short_d16_hi v[2:3], v1, off offset:2176
	v_mul_f32_e32 v1, v33, v73
	v_bfe_u32 v4, v1, 16, 1
	v_add3_u32 v1, v1, v4, s37
	s_cmp_ge_i32 s55, s44
	global_store_short_d16_hi v[2:3], v1, off offset:2240
	s_waitcnt vmcnt(63) expcnt(7) lgkmcnt(15)
	s_barrier
	s_cbranch_scc1 .LBB0_1483
.LBB0_1448:
	v_writelane_b32 v255, s55, 46
	s_cmpk_gt_i32 s55, 0x1ff
	s_cbranch_scc1 .Lattn_nomap
	s_and_b32 s6, s55, 7
	s_bfe_u32 s7, s55, 0x50003
	s_lshl_b32 s6, s6, 1
	s_lshr_b32 s31, s7, 4
	s_add_i32 s6, s6, s31
	s_lshl_b32 s6, s6, 4
	s_and_b32 s7, s7, 15
	s_or_b32 s6, s6, s7
	s_and_b32 s55, s55, 0x100
	s_or_b32 s55, s55, s6

; #define LAS __attribute__((address_space(3)))
; __device__ __forceinline__ void finishSM(f32x16& p0, f32x16& p1, float& l_reg, bf16x8& pa0, bf16x8& pa1, bf16x8& pa2, bf16x8& pa3) {
; #pragma unroll
;     for (int r = 0; r < 16; ++r) p1[r] = __builtin_amdgcn_exp2f(p1[r]);
;     float ps = 0;
; #pragma unroll
;     for (int r = 0; r < 16; ++r) ps += p0[r];
; #pragma unroll
;     for (int r = 0; r < 16; ++r) ps += p1[r];
;     { auto rr = __builtin_amdgcn_permlane32_swap(__float_as_uint(ps), __float_as_uint(ps), false, false);
;       ps = __uint_as_float(rr[0]) + __uint_as_float(rr[1]); }
;     l_reg += ps;
; __device__ __forceinline__ void qkt(f32x16& p0, f32x16& p1, const LAS char* Kl, const bf16x8* qr, const LAS char* Ql, const f32x16& init) {
; #pragma unroll
;     for (int d0 = 0; d0 < 12; ++d0) {
;         const bf16x8 b0 = *reinterpret_cast<const LAS bf16x8*>(Kl + d0 * 32);
;         const bf16x8 b1 = *reinterpret_cast<const LAS bf16x8*>(Kl + 32 * KROWB + d0 * 32);
;         const bf16x8 q = d0 < NQR ? qr[d0 < NQR ? d0 : 0] : *reinterpret_cast<const LAS bf16x8*>(Ql + (d0 - NQR) * 32);
;         p0 = __builtin_amdgcn_mfma_f32_32x32x16_bf16(b0, q, d0 == 0 ? init : p0, 0, 0, 0);
;         p1 = __builtin_amdgcn_mfma_f32_32x32x16_bf16(b1, q, d0 == 0 ? init : p1, 0, 0, 0); }
; }
.LBB0_1464:
	ds_read_b128 v[238:241], v195 offset:58368
	ds_read_b128 v[242:245], v200 offset:38400
	ds_read_b128 v[66:69], v195 offset:58400
	ds_read_b128 v[70:73], v200 offset:38432
	ds_read_b128 v[74:77], v195 offset:58432
	ds_read_b128 v[78:81], v200 offset:38464
	s_waitcnt lgkmcnt(4)
	v_mfma_f32_32x32x16_bf16 v[130:145], v[238:241], v[148:151], v[82:97]
	v_exp_f32_e32 v1, v98
	v_exp_f32_e32 v98, v99
	v_mfma_f32_32x32x16_bf16 v[114:129], v[242:245], v[148:151], v[82:97]
	ds_read_b128 v[238:241], v195 offset:58464
	ds_read_b128 v[242:245], v200 offset:38496
	v_exp_f32_e32 v99, v100
	v_exp_f32_e32 v100, v101
	s_waitcnt lgkmcnt(4)
	v_mfma_f32_32x32x16_bf16 v[130:145], v[66:69], v[152:155], v[130:145]
	v_exp_f32_e32 v101, v102
	v_exp_f32_e32 v102, v103
	v_mfma_f32_32x32x16_bf16 v[114:129], v[70:73], v[152:155], v[114:129]
	ds_read_b128 v[246:249], v189
	ds_read_b128 v[216:219], v189 offset:32
	ds_read_b128 v[66:69], v195 offset:58496
	ds_read_b128 v[70:73], v200 offset:38528
	v_exp_f32_e32 v103, v104
	v_exp_f32_e32 v104, v105
	s_waitcnt lgkmcnt(6)
	v_mfma_f32_32x32x16_bf16 v[130:145], v[74:77], v[156:159], v[130:145]
	v_exp_f32_e32 v105, v106
	v_add_f32_e32 v106, 0, v228
	v_mfma_f32_32x32x16_bf16 v[114:129], v[78:81], v[156:159], v[114:129]
	ds_read_b128 v[74:77], v195 offset:58528
	ds_read_b128 v[78:81], v200 offset:38560
	v_add_f32_e32 v106, v231, v106
	v_add_f32_e32 v106, v229, v106
	v_add_f32_e32 v106, v232, v106
	s_waitcnt lgkmcnt(6)
	v_mfma_f32_32x32x16_bf16 v[130:145], v[238:241], v[160:163], v[130:145]
	v_add_f32_e32 v106, v230, v106
	v_add_f32_e32 v106, v233, v106
	v_add_f32_e32 v106, v226, v106
	v_mfma_f32_32x32x16_bf16 v[114:129], v[242:245], v[160:163], v[114:129]
	ds_read_b128 v[238:241], v195 offset:58560
	ds_read_b128 v[242:245], v200 offset:38592
	v_add_f32_e32 v106, v227, v106
	v_add_f32_e32 v106, v204, v106
	v_add_f32_e32 v106, v206, v106
	s_waitcnt lgkmcnt(4)
	v_mfma_f32_32x32x16_bf16 v[130:145], v[66:69], v[164:167], v[130:145]
	v_add_f32_e32 v106, v205, v106
	v_add_f32_e32 v106, v207, v106
	v_add_f32_e32 v106, v184, v106
	v_mfma_f32_32x32x16_bf16 v[114:129], v[70:73], v[164:167], v[114:129]
	ds_read_b128 v[66:69], v195 offset:58592
	ds_read_b128 v[70:73], v200 offset:38624
	v_add_f32_e32 v106, v202, v106
	v_add_f32_e32 v106, v185, v106
	v_add_f32_e32 v106, v203, v106
	s_waitcnt lgkmcnt(4)
	v_mfma_f32_32x32x16_bf16 v[130:145], v[74:77], v[168:171], v[130:145]
	v_add_f32_e32 v106, v1, v106
	v_add_f32_e32 v106, v98, v106
	v_add_f32_e32 v106, v99, v106
	v_mfma_f32_32x32x16_bf16 v[114:129], v[78:81], v[168:171], v[114:129]
	ds_read_b128 v[74:77], v195 offset:58624
	ds_read_b128 v[78:81], v200 offset:38656
	v_add_f32_e32 v106, v100, v106
	v_add_f32_e32 v106, v101, v106
	v_exp_f32_e32 v146, v107
	s_waitcnt lgkmcnt(4)
	v_mfma_f32_32x32x16_bf16 v[130:145], v[238:241], v[172:175], v[130:145]
	v_add_f32_e32 v106, v102, v106
	v_exp_f32_e32 v208, v108
	v_mfma_f32_32x32x16_bf16 v[114:129], v[242:245], v[172:175], v[114:129]
	ds_read_b128 v[238:241], v195 offset:58656
	ds_read_b128 v[242:245], v200 offset:38688
	v_add_f32_e32 v106, v103, v106
	v_exp_f32_e32 v209, v109
	s_waitcnt lgkmcnt(4)
	v_mfma_f32_32x32x16_bf16 v[130:145], v[66:69], v[176:179], v[130:145]
	v_add_f32_e32 v106, v104, v106
	v_exp_f32_e32 v212, v110
	v_mfma_f32_32x32x16_bf16 v[114:129], v[70:73], v[176:179], v[114:129]
	ds_read_b128 v[66:69], v195 offset:58688
	ds_read_b128 v[70:73], v200 offset:38720
	v_add_f32_e32 v106, v105, v106
	v_add_f32_e32 v106, v146, v106
	s_waitcnt lgkmcnt(4)
	v_mfma_f32_32x32x16_bf16 v[130:145], v[74:77], v[246:249], v[130:145]
	v_add_f32_e32 v106, v208, v106
	v_exp_f32_e32 v222, v113
	v_mfma_f32_32x32x16_bf16 v[114:129], v[78:81], v[246:249], v[114:129]
	ds_read_b128 v[246:249], v189 offset:64
	ds_read_b128 v[74:77], v195 offset:58720
	ds_read_b128 v[78:81], v200 offset:38752
	v_add_f32_e32 v106, v209, v106
	v_add_f32_e32 v106, v212, v106
	s_waitcnt lgkmcnt(5)
	v_mfma_f32_32x32x16_bf16 v[130:145], v[238:241], v[216:219], v[130:145]
	v_mfma_f32_32x32x16_bf16 v[114:129], v[242:245], v[216:219], v[114:129]
	ds_read_b128 v[238:241], v189 offset:96
	v_exp_f32_e32 v218, v111
	s_waitcnt lgkmcnt(3)
	v_mfma_f32_32x32x16_bf16 v[130:145], v[66:69], v[246:249], v[130:145]
	v_exp_f32_e32 v219, v112
	v_mfma_f32_32x32x16_bf16 v[114:129], v[70:73], v[246:249], v[114:129]
	v_add_f32_e32 v106, v218, v106
	s_waitcnt lgkmcnt(0)
; #define LAS __attribute__((address_space(3)))
; __device__ __forceinline__ void finishSM(f32x16& p0, f32x16& p1, float& l_reg, bf16x8& pa0, bf16x8& pa1, bf16x8& pa2, bf16x8& pa3) {
; #pragma unroll
;     for (int r = 0; r < 16; ++r) p1[r] = __builtin_amdgcn_exp2f(p1[r]);
;     float ps = 0;
; #pragma unroll
;     for (int r = 0; r < 16; ++r) ps += p0[r];
; #pragma unroll
;     for (int r = 0; r < 16; ++r) ps += p1[r];
;     { auto rr = __builtin_amdgcn_permlane32_swap(__float_as_uint(ps), __float_as_uint(ps), false, false);
;       ps = __uint_as_float(rr[0]) + __uint_as_float(rr[1]); }
;     l_reg += ps;
;     ...
;     PK4(p0, 0, pa0); PK4(p0, 8, pa1); PK4(p1, 0, pa2); PK4(p1, 8, pa3);
;     ...
; }
; __device__ __forceinline__ void qkt(f32x16& p0, f32x16& p1, const LAS char* Kl, const bf16x8* qr, const LAS char* Ql, const f32x16& init) {
; #pragma unroll
;     for (int d0 = 0; d0 < 12; ++d0) {
;         const bf16x8 b0 = *reinterpret_cast<const LAS bf16x8*>(Kl + d0 * 32);
;         const bf16x8 b1 = *reinterpret_cast<const LAS bf16x8*>(Kl + 32 * KROWB + d0 * 32);
;         const bf16x8 q = d0 < NQR ? qr[d0 < NQR ? d0 : 0] : *reinterpret_cast<const LAS bf16x8*>(Ql + (d0 - NQR) * 32);
;         p0 = __builtin_amdgcn_mfma_f32_32x32x16_bf16(b0, q, d0 == 0 ? init : p0, 0, 0, 0);
;         p1 = __builtin_amdgcn_mfma_f32_32x32x16_bf16(b1, q, d0 == 0 ? init : p1, 0, 0, 0); }
; }
; __device__ __forceinline__ int v_st(int k, int c) { const int kk = (k & ~0xC) | ((k & 4) << 1) | ((k & 8) >> 1); return ((kk >> 3) * 4 + (c >> 5)) * 512 + ((kk & 7) * 32 + (c & 31)) * 2; }
; __device__ __forceinline__ int v_rd_base(int lane) { return ((lane & 3) << 3) | (((lane >> 2) & 3) << 6) | (((lane >> 4) & 1) << 5) | (((lane >> 5) & 1) << 8); }
; template <int OFF> __device__ __forceinline__ s16x4 tr_read(int vb) {
;     s16x4 r; asm volatile("ds_read_b64_tr_b16 %0, %1 offset:%2" : "=&v"(r) : "v"(vb), "i"(OFF) : "memory"); return r;
; }
; template <int D0> __device__ __forceinline__ void pv_one(f32x16& od, int vb, bf16x8 pa0, bf16x8 pa1, bf16x8 pa2, bf16x8 pa3) {
;     const s16x4 l0 = tr_read<v_rd_off(D0, 0, 0)>(vb), h0 = tr_read<v_rd_off(D0, 0, 1)>(vb), l1 = tr_read<v_rd_off(D0, 1, 0)>(vb), h1 = tr_read<v_rd_off(D0, 1, 1)>(vb);
;     const s16x4 l2 = tr_read<v_rd_off(D0, 2, 0)>(vb), h2 = tr_read<v_rd_off(D0, 2, 1)>(vb), l3 = tr_read<v_rd_off(D0, 3, 0)>(vb), h3 = tr_read<v_rd_off(D0, 3, 1)>(vb);
	v_mfma_f32_32x32x16_bf16 v[130:145], v[74:77], v[238:241], v[130:145]
	v_add_f32_e32 v106, v219, v106
	v_mfma_f32_32x32x16_bf16 v[114:129], v[78:81], v[238:241], v[114:129]
	v_add_f32_e32 v106, v222, v106
	v_mov_b32_e32 v107, v106
	s_nop 1
	v_permlane32_swap_b32_e32 v106, v107
	v_add_f32_e32 v106, v106, v107
	v_add_f32_e32 v201, v201, v106
	v_cvt_pk_bf16_f32 v106, v228, v231
	v_cvt_pk_bf16_f32 v107, v229, v232
	v_cvt_pk_bf16_f32 v108, v230, v233
	v_cvt_pk_bf16_f32 v109, v226, v227
	v_cvt_pk_bf16_f32 v110, v204, v206
	v_cvt_pk_bf16_f32 v111, v205, v207
	v_cvt_pk_bf16_f32 v112, v184, v202
	v_cvt_pk_bf16_f32 v113, v185, v203
	s_nop 0
	v_permlane32_swap_b32_e32 v106, v108
	v_cvt_pk_bf16_f32 v202, v1, v98
	v_cvt_pk_bf16_f32 v203, v99, v100
	v_cvt_pk_bf16_f32 v204, v101, v102
	v_cvt_pk_bf16_f32 v205, v103, v104
	v_cvt_pk_bf16_f32 v216, v105, v146
	v_cvt_pk_bf16_f32 v217, v208, v209
	v_cvt_pk_bf16_f32 v218, v212, v218
	v_cvt_pk_bf16_f32 v219, v219, v222
	v_permlane32_swap_b32_e32 v107, v109
	v_permlane32_swap_b32_e32 v110, v112
	v_permlane32_swap_b32_e32 v111, v113
	v_permlane32_swap_b32_e32 v202, v204
	v_permlane32_swap_b32_e32 v203, v205
	v_permlane32_swap_b32_e32 v216, v218
	v_permlane32_swap_b32_e32 v217, v219
	v_lshl_add_u64 v[184:185], s[2:3], 0, v[182:183]
	s_mov_b32 s10, 0x46508000
	v_add_co_u32_e32 v98, vcc, s10, v184
	s_mov_b32 s10, 0x4650a000
	s_nop 0
	v_addc_co_u32_e32 v99, vcc, 0, v185, vcc
	v_add_co_u32_e32 v102, vcc, s10, v184
	s_nop 1
	v_addc_co_u32_e32 v103, vcc, 0, v185, vcc
	global_load_dwordx4 v[98:101], v[98:99], off
	s_nop 0
	global_load_dwordx4 v[102:105], v[102:103], off
	ds_read_b64_tr_b16 v[226:227], v197 offset:0
	ds_read_b64_tr_b16 v[228:229], v197 offset:0x800
	ds_read_b64_tr_b16 v[230:231], v197 offset:0x1000
	ds_read_b64_tr_b16 v[232:233], v197 offset:0x1800
	ds_read_b64_tr_b16 v[238:239], v197 offset:0x2000
	ds_read_b64_tr_b16 v[240:241], v197 offset:0x2800
	ds_read_b64_tr_b16 v[242:243], v197 offset:0x3000
	ds_read_b64_tr_b16 v[244:245], v197 offset:0x3800
	s_waitcnt lgkmcnt(0)
	s_nop 0
	v_mfma_f32_32x32x16_bf16 v[2:17], v[106:109], v[226:229], v[2:17]
	ds_read_b64_tr_b16 v[226:227], v197 offset:0x200
	ds_read_b64_tr_b16 v[228:229], v197 offset:0xa00
	v_mfma_f32_32x32x16_bf16 v[2:17], v[110:113], v[230:233], v[2:17]
	ds_read_b64_tr_b16 v[230:231], v197 offset:0x1200
	ds_read_b64_tr_b16 v[232:233], v197 offset:0x1a00
	v_mfma_f32_32x32x16_bf16 v[2:17], v[202:205], v[238:241], v[2:17]
	ds_read_b64_tr_b16 v[238:239], v197 offset:0x2200
	ds_read_b64_tr_b16 v[240:241], v197 offset:0x2a00
	v_mfma_f32_32x32x16_bf16 v[2:17], v[216:219], v[242:245], v[2:17]
	ds_read_b64_tr_b16 v[242:243], v197 offset:0x3200
	ds_read_b64_tr_b16 v[244:245], v197 offset:0x3a00
	s_waitcnt lgkmcnt(0)
	v_mfma_f32_32x32x16_bf16 v[50:65], v[106:109], v[226:229], v[50:65]
	ds_read_b64_tr_b16 v[226:227], v197 offset:0x400
	ds_read_b64_tr_b16 v[228:229], v197 offset:0xc00
	v_mfma_f32_32x32x16_bf16 v[50:65], v[110:113], v[230:233], v[50:65]
	ds_read_b64_tr_b16 v[230:231], v197 offset:0x1400
	ds_read_b64_tr_b16 v[232:233], v197 offset:0x1c00
	v_mfma_f32_32x32x16_bf16 v[50:65], v[202:205], v[238:241], v[50:65]
	ds_read_b64_tr_b16 v[238:239], v197 offset:0x2400
	ds_read_b64_tr_b16 v[240:241], v197 offset:0x2c00
	v_mfma_f32_32x32x16_bf16 v[50:65], v[216:219], v[242:245], v[50:65]
	ds_read_b64_tr_b16 v[242:243], v197 offset:0x3400
	ds_read_b64_tr_b16 v[244:245], v197 offset:0x3c00
	s_waitcnt lgkmcnt(0)
	v_mfma_f32_32x32x16_bf16 v[34:49], v[106:109], v[226:229], v[34:49]
	ds_read_b64_tr_b16 v[226:227], v197 offset:0x600
	ds_read_b64_tr_b16 v[228:229], v197 offset:0xe00
	v_mfma_f32_32x32x16_bf16 v[34:49], v[110:113], v[230:233], v[34:49]
	ds_read_b64_tr_b16 v[230:231], v197 offset:0x1600
	ds_read_b64_tr_b16 v[232:233], v197 offset:0x1e00
	v_mfma_f32_32x32x16_bf16 v[34:49], v[202:205], v[238:241], v[34:49]
	ds_read_b64_tr_b16 v[238:239], v197 offset:0x2600
	ds_read_b64_tr_b16 v[240:241], v197 offset:0x2e00
	v_mfma_f32_32x32x16_bf16 v[34:49], v[216:219], v[242:245], v[34:49]
	ds_read_b64_tr_b16 v[242:243], v197 offset:0x3600
	ds_read_b64_tr_b16 v[244:245], v197 offset:0x3e00
	s_waitcnt lgkmcnt(0)
	v_mfma_f32_32x32x16_bf16 v[18:33], v[106:109], v[226:229], v[18:33]
	v_max3_f32 v1, v130, v131, v132
	v_max3_f32 v106, v114, v115, v116
	v_max3_f32 v1, v1, v133, v134
	v_max3_f32 v106, v106, v117, v118
	v_max3_f32 v1, v1, v135, v136
	v_max3_f32 v106, v106, v119, v120
	v_max3_f32 v1, v1, v137, v138
	v_mfma_f32_32x32x16_bf16 v[18:33], v[110:113], v[230:233], v[18:33]
	v_max3_f32 v106, v106, v121, v122
	v_max3_f32 v1, v1, v139, v140
	v_max3_f32 v106, v106, v123, v124
	v_max3_f32 v1, v1, v141, v142
	v_max3_f32 v106, v106, v125, v126
	v_max_f32_e32 v107, v129, v129
	v_max_f32_e32 v108, v145, v145
	v_mfma_f32_32x32x16_bf16 v[18:33], v[202:205], v[238:241], v[18:33]
	v_max3_f32 v1, v1, v143, v144
	v_max3_f32 v106, v106, v127, v128
	v_max_f32_e32 v107, v108, v107
	v_max3_f32 v1, v1, v106, v107
	v_mov_b32_e32 v106, v1
	s_nop 1
	v_permlane32_swap_b32_e32 v1, v106
	v_mfma_f32_32x32x16_bf16 v[18:33], v[216:219], v[242:245], v[18:33]
	v_max_f32_e32 v106, v106, v106
	v_max_f32_e32 v1, v1, v1
	v_max_f32_e32 v106, v1, v106
	v_cmp_ge_f32_e32 vcc, s12, v106
	s_cmp_eq_u64 vcc, exec
	s_cbranch_scc0 .LBB0_1471

; #define LAS __attribute__((address_space(3)))
; __device__ __forceinline__ void finishSM(f32x16& p0, f32x16& p1, float& l_reg, bf16x8& pa0, bf16x8& pa1, bf16x8& pa2, bf16x8& pa3) {
; #pragma unroll
;     for (int r = 0; r < 16; ++r) p1[r] = __builtin_amdgcn_exp2f(p1[r]);
;     float ps = 0;
; #pragma unroll
;     for (int r = 0; r < 16; ++r) ps += p0[r];
; #pragma unroll
;     for (int r = 0; r < 16; ++r) ps += p1[r];
;     { auto rr = __builtin_amdgcn_permlane32_swap(__float_as_uint(ps), __float_as_uint(ps), false, false);
;       ps = __uint_as_float(rr[0]) + __uint_as_float(rr[1]); }
;     l_reg += ps;
; __device__ __forceinline__ void qkt(f32x16& p0, f32x16& p1, const LAS char* Kl, const bf16x8* qr, const LAS char* Ql, const f32x16& init) {
; #pragma unroll
;     for (int d0 = 0; d0 < 12; ++d0) {
;         const bf16x8 b0 = *reinterpret_cast<const LAS bf16x8*>(Kl + d0 * 32);
;         const bf16x8 b1 = *reinterpret_cast<const LAS bf16x8*>(Kl + 32 * KROWB + d0 * 32);
;         const bf16x8 q = d0 < NQR ? qr[d0 < NQR ? d0 : 0] : *reinterpret_cast<const LAS bf16x8*>(Ql + (d0 - NQR) * 32);
;         p0 = __builtin_amdgcn_mfma_f32_32x32x16_bf16(b0, q, d0 == 0 ? init : p0, 0, 0, 0);
;         p1 = __builtin_amdgcn_mfma_f32_32x32x16_bf16(b1, q, d0 == 0 ? init : p1, 0, 0, 0); }
; }
.LBB0_1468:
	ds_read_b128 v[202:205], v195 offset:32768
	ds_read_b128 v[216:219], v195 offset:45568
	ds_read_b128 v[66:69], v195 offset:32800
	ds_read_b128 v[70:73], v195 offset:45600
	ds_read_b128 v[74:77], v195 offset:32832
	ds_read_b128 v[78:81], v195 offset:45632
	v_exp_f32_e32 v1, v130
	v_exp_f32_e32 v146, v131
	v_exp_f32_e32 v206, v132
	v_exp_f32_e32 v207, v133
	v_exp_f32_e32 v208, v134
	v_exp_f32_e32 v209, v135
	v_exp_f32_e32 v212, v136
	v_exp_f32_e32 v222, v137
	v_exp_f32_e32 v223, v138
	v_exp_f32_e32 v238, v139
	v_exp_f32_e32 v239, v140
	v_exp_f32_e32 v240, v141
	v_exp_f32_e32 v241, v142
	v_exp_f32_e32 v242, v143
	v_exp_f32_e32 v243, v144
	v_exp_f32_e32 v244, v145
	s_waitcnt lgkmcnt(4)
	v_mfma_f32_32x32x16_bf16 v[130:145], v[202:205], v[148:151], v[82:97]
	v_exp_f32_e32 v114, v114
	v_mfma_f32_32x32x16_bf16 v[98:113], v[216:219], v[148:151], v[82:97]
	ds_read_b128 v[202:205], v195 offset:32864
	ds_read_b128 v[216:219], v195 offset:45664
	v_exp_f32_e32 v115, v115
	s_waitcnt lgkmcnt(4)
	v_mfma_f32_32x32x16_bf16 v[130:145], v[66:69], v[152:155], v[130:145]
	v_exp_f32_e32 v116, v116
	v_mfma_f32_32x32x16_bf16 v[98:113], v[70:73], v[152:155], v[98:113]
	ds_read_b128 v[226:229], v189
	ds_read_b128 v[230:233], v189 offset:32
	ds_read_b128 v[66:69], v195 offset:32896
	ds_read_b128 v[70:73], v195 offset:45696
	v_exp_f32_e32 v117, v117
	s_waitcnt lgkmcnt(6)
	v_mfma_f32_32x32x16_bf16 v[130:145], v[74:77], v[156:159], v[130:145]
	v_exp_f32_e32 v118, v118
	v_mfma_f32_32x32x16_bf16 v[98:113], v[78:81], v[156:159], v[98:113]
	ds_read_b128 v[246:249], v189 offset:64
	ds_read_b128 v[74:77], v195 offset:32928
	ds_read_b128 v[78:81], v195 offset:45728
	v_exp_f32_e32 v119, v119
	s_waitcnt lgkmcnt(7)
	v_mfma_f32_32x32x16_bf16 v[130:145], v[202:205], v[160:163], v[130:145]
	v_exp_f32_e32 v120, v120
	v_mfma_f32_32x32x16_bf16 v[98:113], v[216:219], v[160:163], v[98:113]
	ds_read_b128 v[202:205], v195 offset:32960
	ds_read_b128 v[216:219], v195 offset:45760
	v_exp_f32_e32 v121, v121
	s_waitcnt lgkmcnt(5)
	v_mfma_f32_32x32x16_bf16 v[130:145], v[66:69], v[164:167], v[130:145]
	v_exp_f32_e32 v245, v122
	v_mfma_f32_32x32x16_bf16 v[98:113], v[70:73], v[164:167], v[98:113]
	ds_read_b128 v[66:69], v195 offset:32992
	ds_read_b128 v[70:73], v195 offset:45792
	v_add_f32_e32 v122, 0, v1
	v_add_f32_e32 v122, v146, v122
	s_waitcnt lgkmcnt(4)
	v_mfma_f32_32x32x16_bf16 v[130:145], v[74:77], v[168:171], v[130:145]
	v_add_f32_e32 v122, v206, v122
	v_add_f32_e32 v122, v207, v122
	v_mfma_f32_32x32x16_bf16 v[98:113], v[78:81], v[168:171], v[98:113]
	ds_read_b128 v[74:77], v195 offset:33024
	ds_read_b128 v[78:81], v195 offset:45824
	v_add_f32_e32 v122, v208, v122
	v_add_f32_e32 v122, v209, v122
	s_waitcnt lgkmcnt(4)
	v_mfma_f32_32x32x16_bf16 v[130:145], v[202:205], v[172:175], v[130:145]
	v_add_f32_e32 v122, v212, v122
	v_add_f32_e32 v122, v222, v122
	v_mfma_f32_32x32x16_bf16 v[98:113], v[216:219], v[172:175], v[98:113]
	ds_read_b128 v[202:205], v195 offset:33056
	ds_read_b128 v[216:219], v195 offset:45856
	v_add_f32_e32 v122, v223, v122
	v_add_f32_e32 v122, v238, v122
	s_waitcnt lgkmcnt(4)
	v_mfma_f32_32x32x16_bf16 v[130:145], v[66:69], v[176:179], v[130:145]
	v_add_f32_e32 v122, v239, v122
	v_add_f32_e32 v122, v240, v122
	v_mfma_f32_32x32x16_bf16 v[98:113], v[70:73], v[176:179], v[98:113]
	ds_read_b128 v[66:69], v195 offset:33088
	ds_read_b128 v[70:73], v195 offset:45888
	v_add_f32_e32 v122, v241, v122
	v_add_f32_e32 v122, v242, v122
	s_waitcnt lgkmcnt(4)
	v_mfma_f32_32x32x16_bf16 v[130:145], v[74:77], v[226:229], v[130:145]
	v_add_f32_e32 v122, v243, v122
	v_add_f32_e32 v122, v244, v122
	v_mfma_f32_32x32x16_bf16 v[98:113], v[78:81], v[226:229], v[98:113]
	ds_read_b128 v[226:229], v189 offset:96
	ds_read_b128 v[74:77], v195 offset:33120
	ds_read_b128 v[78:81], v195 offset:45920
	v_add_f32_e32 v122, v114, v122
	v_add_f32_e32 v122, v115, v122
	s_waitcnt lgkmcnt(5)
	v_mfma_f32_32x32x16_bf16 v[130:145], v[202:205], v[230:233], v[130:145]
	v_add_f32_e32 v122, v116, v122
	v_add_f32_e32 v122, v117, v122
	v_mfma_f32_32x32x16_bf16 v[98:113], v[216:219], v[230:233], v[98:113]
	v_add_f32_e32 v122, v118, v122
	v_exp_f32_e32 v217, v123
	s_waitcnt lgkmcnt(3)
	v_mfma_f32_32x32x16_bf16 v[130:145], v[66:69], v[246:249], v[130:145]
	v_add_f32_e32 v122, v119, v122
	v_exp_f32_e32 v218, v124
	v_mfma_f32_32x32x16_bf16 v[98:113], v[70:73], v[246:249], v[98:113]
	v_add_f32_e32 v122, v120, v122
	v_exp_f32_e32 v219, v125
	s_waitcnt lgkmcnt(0)
; #define LAS __attribute__((address_space(3)))
; __device__ __forceinline__ void finishSM(f32x16& p0, f32x16& p1, float& l_reg, bf16x8& pa0, bf16x8& pa1, bf16x8& pa2, bf16x8& pa3) {
; #pragma unroll
;     for (int r = 0; r < 16; ++r) p1[r] = __builtin_amdgcn_exp2f(p1[r]);
;     float ps = 0;
; #pragma unroll
;     for (int r = 0; r < 16; ++r) ps += p0[r];
; #pragma unroll
;     for (int r = 0; r < 16; ++r) ps += p1[r];
;     { auto rr = __builtin_amdgcn_permlane32_swap(__float_as_uint(ps), __float_as_uint(ps), false, false);
;       ps = __uint_as_float(rr[0]) + __uint_as_float(rr[1]); }
;     l_reg += ps;
;     ...
;     PK4(p0, 0, pa0); PK4(p0, 8, pa1); PK4(p1, 0, pa2); PK4(p1, 8, pa3);
;     ...
; }
; __device__ __forceinline__ void qkt(f32x16& p0, f32x16& p1, const LAS char* Kl, const bf16x8* qr, const LAS char* Ql, const f32x16& init) {
; #pragma unroll
;     for (int d0 = 0; d0 < 12; ++d0) {
;         const bf16x8 b0 = *reinterpret_cast<const LAS bf16x8*>(Kl + d0 * 32);
;         const bf16x8 b1 = *reinterpret_cast<const LAS bf16x8*>(Kl + 32 * KROWB + d0 * 32);
;         const bf16x8 q = d0 < NQR ? qr[d0 < NQR ? d0 : 0] : *reinterpret_cast<const LAS bf16x8*>(Ql + (d0 - NQR) * 32);
;         p0 = __builtin_amdgcn_mfma_f32_32x32x16_bf16(b0, q, d0 == 0 ? init : p0, 0, 0, 0);
;         p1 = __builtin_amdgcn_mfma_f32_32x32x16_bf16(b1, q, d0 == 0 ? init : p1, 0, 0, 0); }
; }
; __device__ __forceinline__ int v_st(int k, int c) { const int kk = (k & ~0xC) | ((k & 4) << 1) | ((k & 8) >> 1); return ((kk >> 3) * 4 + (c >> 5)) * 512 + ((kk & 7) * 32 + (c & 31)) * 2; }
; __device__ __forceinline__ int v_rd_base(int lane) { return ((lane & 3) << 3) | (((lane >> 2) & 3) << 6) | (((lane >> 4) & 1) << 5) | (((lane >> 5) & 1) << 8); }
; template <int OFF> __device__ __forceinline__ s16x4 tr_read(int vb) {
;     s16x4 r; asm volatile("ds_read_b64_tr_b16 %0, %1 offset:%2" : "=&v"(r) : "v"(vb), "i"(OFF) : "memory"); return r;
; }
; template <int D0> __device__ __forceinline__ void pv_one(f32x16& od, int vb, bf16x8 pa0, bf16x8 pa1, bf16x8 pa2, bf16x8 pa3) {
;     const s16x4 l0 = tr_read<v_rd_off(D0, 0, 0)>(vb), h0 = tr_read<v_rd_off(D0, 0, 1)>(vb), l1 = tr_read<v_rd_off(D0, 1, 0)>(vb), h1 = tr_read<v_rd_off(D0, 1, 1)>(vb);
;     const s16x4 l2 = tr_read<v_rd_off(D0, 2, 0)>(vb), h2 = tr_read<v_rd_off(D0, 2, 1)>(vb), l3 = tr_read<v_rd_off(D0, 3, 0)>(vb), h3 = tr_read<v_rd_off(D0, 3, 1)>(vb);
	v_mfma_f32_32x32x16_bf16 v[130:145], v[74:77], v[226:229], v[130:145]
	v_add_f32_e32 v122, v121, v122
	v_mfma_f32_32x32x16_bf16 v[98:113], v[78:81], v[226:229], v[98:113]
	v_exp_f32_e32 v226, v126
	v_add_f32_e32 v122, v245, v122
	v_exp_f32_e32 v227, v127
	v_add_f32_e32 v122, v217, v122
	v_exp_f32_e32 v228, v128
	v_add_f32_e32 v122, v218, v122
	v_exp_f32_e32 v229, v129
	v_add_f32_e32 v122, v219, v122
	v_add_f32_e32 v122, v226, v122
	v_add_f32_e32 v122, v227, v122
	v_add_f32_e32 v122, v228, v122
	v_add_f32_e32 v122, v229, v122
	v_mov_b32_e32 v123, v122
	s_nop 1
	v_permlane32_swap_b32_e32 v122, v123
	v_add_f32_e32 v122, v122, v123
	v_add_f32_e32 v201, v201, v122
	v_cvt_pk_bf16_f32 v122, v1, v146
	v_cvt_pk_bf16_f32 v123, v206, v207
	v_cvt_pk_bf16_f32 v124, v208, v209
	v_cvt_pk_bf16_f32 v125, v212, v222
	v_cvt_pk_bf16_f32 v126, v223, v238
	v_cvt_pk_bf16_f32 v127, v239, v240
	v_cvt_pk_bf16_f32 v128, v241, v242
	v_cvt_pk_bf16_f32 v129, v243, v244
	s_nop 0
	v_permlane32_swap_b32_e32 v122, v124
	v_cvt_pk_bf16_f32 v202, v114, v115
	v_cvt_pk_bf16_f32 v203, v116, v117
	v_cvt_pk_bf16_f32 v204, v118, v119
	v_cvt_pk_bf16_f32 v205, v120, v121
	v_cvt_pk_bf16_f32 v216, v245, v217
	v_cvt_pk_bf16_f32 v217, v218, v219
	v_cvt_pk_bf16_f32 v218, v226, v227
	v_cvt_pk_bf16_f32 v219, v228, v229
	v_permlane32_swap_b32_e32 v123, v125
	v_permlane32_swap_b32_e32 v126, v128
	v_permlane32_swap_b32_e32 v127, v129
	v_permlane32_swap_b32_e32 v202, v204
	v_permlane32_swap_b32_e32 v203, v205
	v_permlane32_swap_b32_e32 v216, v218
	v_permlane32_swap_b32_e32 v217, v219
	s_mov_b32 s10, 0x4650c000
	v_add_co_u32_e32 v114, vcc, s10, v184
	s_mov_b32 s10, 0x4650e000
	s_nop 0
	v_addc_co_u32_e32 v115, vcc, 0, v185, vcc
	v_add_co_u32_e32 v118, vcc, s10, v184
	s_nop 1
	v_addc_co_u32_e32 v119, vcc, 0, v185, vcc
	global_load_dwordx4 v[114:117], v[114:115], off
	s_nop 0
	global_load_dwordx4 v[118:121], v[118:119], off
	ds_read_b64_tr_b16 v[226:227], v191 offset:0
	ds_read_b64_tr_b16 v[228:229], v191 offset:0x800
	ds_read_b64_tr_b16 v[230:231], v191 offset:0x1000
	ds_read_b64_tr_b16 v[232:233], v191 offset:0x1800
	ds_read_b64_tr_b16 v[238:239], v191 offset:0x2000
	ds_read_b64_tr_b16 v[240:241], v191 offset:0x2800
	ds_read_b64_tr_b16 v[242:243], v191 offset:0x3000
	ds_read_b64_tr_b16 v[244:245], v191 offset:0x3800
	s_waitcnt lgkmcnt(0)
	s_nop 0
	v_mfma_f32_32x32x16_bf16 v[2:17], v[122:125], v[226:229], v[2:17]
	ds_read_b64_tr_b16 v[226:227], v191 offset:0x200
	ds_read_b64_tr_b16 v[228:229], v191 offset:0xa00
	v_mfma_f32_32x32x16_bf16 v[2:17], v[126:129], v[230:233], v[2:17]
	ds_read_b64_tr_b16 v[230:231], v191 offset:0x1200
	ds_read_b64_tr_b16 v[232:233], v191 offset:0x1a00
	v_mfma_f32_32x32x16_bf16 v[2:17], v[202:205], v[238:241], v[2:17]
	ds_read_b64_tr_b16 v[238:239], v191 offset:0x2200
	ds_read_b64_tr_b16 v[240:241], v191 offset:0x2a00
	v_mfma_f32_32x32x16_bf16 v[2:17], v[216:219], v[242:245], v[2:17]
	ds_read_b64_tr_b16 v[242:243], v191 offset:0x3200
	ds_read_b64_tr_b16 v[244:245], v191 offset:0x3a00
	s_waitcnt lgkmcnt(0)
	v_mfma_f32_32x32x16_bf16 v[50:65], v[122:125], v[226:229], v[50:65]
	ds_read_b64_tr_b16 v[226:227], v191 offset:0x400
	ds_read_b64_tr_b16 v[228:229], v191 offset:0xc00
	v_mfma_f32_32x32x16_bf16 v[50:65], v[126:129], v[230:233], v[50:65]
	ds_read_b64_tr_b16 v[230:231], v191 offset:0x1400
	ds_read_b64_tr_b16 v[232:233], v191 offset:0x1c00
	v_mfma_f32_32x32x16_bf16 v[50:65], v[202:205], v[238:241], v[50:65]
	ds_read_b64_tr_b16 v[238:239], v191 offset:0x2400
	ds_read_b64_tr_b16 v[240:241], v191 offset:0x2c00
	v_mfma_f32_32x32x16_bf16 v[50:65], v[216:219], v[242:245], v[50:65]
	ds_read_b64_tr_b16 v[242:243], v191 offset:0x3400
	ds_read_b64_tr_b16 v[244:245], v191 offset:0x3c00
	s_waitcnt lgkmcnt(0)
	v_mfma_f32_32x32x16_bf16 v[34:49], v[122:125], v[226:229], v[34:49]
	ds_read_b64_tr_b16 v[226:227], v191 offset:0x600
	ds_read_b64_tr_b16 v[228:229], v191 offset:0xe00
	v_mfma_f32_32x32x16_bf16 v[34:49], v[126:129], v[230:233], v[34:49]
	ds_read_b64_tr_b16 v[230:231], v191 offset:0x1600
	ds_read_b64_tr_b16 v[232:233], v191 offset:0x1e00
	v_mfma_f32_32x32x16_bf16 v[34:49], v[202:205], v[238:241], v[34:49]
	ds_read_b64_tr_b16 v[238:239], v191 offset:0x2600
	ds_read_b64_tr_b16 v[240:241], v191 offset:0x2e00
	v_mfma_f32_32x32x16_bf16 v[34:49], v[216:219], v[242:245], v[34:49]
	ds_read_b64_tr_b16 v[242:243], v191 offset:0x3600
	ds_read_b64_tr_b16 v[244:245], v191 offset:0x3e00
	s_waitcnt lgkmcnt(0)
	v_mfma_f32_32x32x16_bf16 v[18:33], v[122:125], v[226:229], v[18:33]
	v_max3_f32 v1, v130, v131, v132
	v_max3_f32 v122, v98, v99, v100
	v_max3_f32 v1, v1, v133, v134
	v_max3_f32 v122, v122, v101, v102
	v_max3_f32 v1, v1, v135, v136
	v_max3_f32 v122, v122, v103, v104
	v_max3_f32 v1, v1, v137, v138
	v_mfma_f32_32x32x16_bf16 v[18:33], v[126:129], v[230:233], v[18:33]
	v_max3_f32 v122, v122, v105, v106
	v_max3_f32 v1, v1, v139, v140
	v_max3_f32 v122, v122, v107, v108
	v_max3_f32 v1, v1, v141, v142
	v_max3_f32 v122, v122, v109, v110
	v_max_f32_e32 v123, v113, v113
	v_max_f32_e32 v124, v145, v145
	v_mfma_f32_32x32x16_bf16 v[18:33], v[202:205], v[238:241], v[18:33]
	v_max3_f32 v1, v1, v143, v144
	v_max3_f32 v122, v122, v111, v112
	v_max_f32_e32 v123, v124, v123
	v_max3_f32 v1, v1, v122, v123
	v_mov_b32_e32 v122, v1
	s_nop 1
	v_permlane32_swap_b32_e32 v1, v122
	v_mfma_f32_32x32x16_bf16 v[18:33], v[216:219], v[242:245], v[18:33]
	v_max_f32_e32 v122, v122, v122
	v_max_f32_e32 v1, v1, v1
	v_max_f32_e32 v122, v1, v122
	v_cmp_ge_f32_e32 vcc, s12, v122
	s_cmp_eq_u64 vcc, exec
	s_cbranch_scc0 .LBB0_1474
	s_mov_b64 s[16:17], 0x8000
.LBB0_1470:
	v_exp_f32_e32 v228, v130
	v_exp_f32_e32 v231, v131
	v_exp_f32_e32 v229, v132
	v_exp_f32_e32 v232, v133
	v_exp_f32_e32 v230, v134
	v_exp_f32_e32 v233, v135
	v_exp_f32_e32 v226, v136
	v_exp_f32_e32 v227, v137
	v_exp_f32_e32 v204, v138
	v_exp_f32_e32 v206, v139
	v_exp_f32_e32 v205, v140
	v_exp_f32_e32 v207, v141
	v_exp_f32_e32 v184, v142
	v_exp_f32_e32 v202, v143
	v_exp_f32_e32 v185, v144
	v_exp_f32_e32 v203, v145
	s_waitcnt vmcnt(2)
	s_add_u32 s60, s60, 0xc000
	s_addc_u32 s59, s59, 0
	s_add_i32 s65, s65, 2
	s_cmp_ge_u32 s65, s57
	v_lshl_add_u64 v[182:183], v[182:183], 0, s[16:17]
	s_waitcnt vmcnt(0)
	s_barrier
	s_cbranch_scc0 .LBB0_1462
	v_mov_b64_e32 v[66:67], v[82:83]
	v_mov_b64_e32 v[68:69], v[84:85]
	v_mov_b64_e32 v[70:71], v[86:87]
	v_mov_b64_e32 v[72:73], v[88:89]
	v_mov_b64_e32 v[74:75], v[90:91]
	v_mov_b64_e32 v[76:77], v[92:93]
	v_mov_b64_e32 v[78:79], v[94:95]
	v_mov_b64_e32 v[80:81], v[96:97]
	s_branch .LBB0_1477
